# attention first key tile of each 32-query sub-block: same de-serialization of the 16 exec-masked LDS bias reads (unconditional reads, one wait, mask-select)
# speedup vs baseline: 1.0135x; 1.0018x over previous
; #define LAS __attribute__((address_space(3)))
; DI float kf(float c) { asm volatile("" : "+v"(c)); return c; }
; DI int crow(int reg, int h) { return (reg & 3) + 8 * (reg >> 2) + 4 * h; }
; DI void phase_attn(const Frame& F, int j) {
;     ...
;             bf16x8 Qf[4];
; #pragma unroll
;             for (int s = 0; s < 4; ++s) Qf[s] = *(const bf16x8*)(QKV + qrow * QKV_N + head * 64 + 16 * s + 8 * h);
;             f32x16 O0, O1;
; #pragma unroll
;             for (int i = 0; i < 16; ++i) { O0[i] = 0.f; O1[i] = 0.f; }
;             float mrun = sink, lrun = h ? 0.f : 1.f;
;             for (int kt = sub; kt < sub + 9; ++kt) {
;                 f32x16 x;
; #pragma unroll
;                 for (int i = 0; i < 16; ++i) x[i] = 0.f;
; #pragma unroll
;                 for (int s = 0; s < 4; ++s) { const bf16x8 kf = *(const LAS bf16x8*)(Ks + (32 * kt + r) * KS_STRIDE + 16 * s + 8 * h);
;                     x = __builtin_amdgcn_mfma_f32_32x32x16_bf16(kf, Qf[s], x, 0, 0, 0); }
;                 s16x4 vf[2][4];
; #pragma unroll
;                 for (int s = 0; s < 2; ++s) { const int kc = 32 * kt + 16 * s + 4 * h;
;                     vf[s][0] = *(const LAS s16x4*)(Vt + r * VT_STRIDE + kc); vf[s][1] = *(const LAS s16x4*)(Vt + r * VT_STRIDE + kc + 8);
;                     vf[s][2] = *(const LAS s16x4*)(Vt + (32 + r) * VT_STRIDE + kc); vf[s][3] = *(const LAS s16x4*)(Vt + (32 + r) * VT_STRIDE + kc + 8); }
;                 __builtin_amdgcn_sched_barrier(0);
;                 float mt = -3.0e38f;
;                 if (kt > sub && kt < sub + 8 && qb > 0 && qb < 31) {
;                     const LAS float* bp = bT + hh * 260 + 32 * kt - 32 * sub - r + 4 * h;
; #pragma unroll
;                     for (int i = 0; i < 16; ++i) { const float sc = x[i] * (0.125f * 1.44269504f) + bp[(i & 3) + 8 * (i >> 2)]; x[i] = sc; mt = fmaxf(mt, sc); }
;                 } else {
; #pragma unroll
;                 for (int i = 0; i < 16; ++i) { const int kl = 32 * kt + crow(i, h); const int rel = kl - 128 - qrel; const int kp = q0 - 128 + kl;
;                     const bool ok = rel >= -128 && rel <= 128 && kp >= 0 && kp < SEQ;
;                     const int bi = rel < -128 ? 0 : (rel > 128 ? 256 : rel + 128);
;                     const float sc = ok ? x[i] * (0.125f * 1.44269504f) + bT[hh * 260 + bi] : -1e30f; x[i] = sc; mt = fmaxf(mt, sc); }
.LBB0_320:
	s_lshl_b32 s2, s82, 5
	v_or_b32_e32 v0, s2, v85
	v_or_b32_e32 v94, s9, v0
	v_mad_i64_i32 v[20:21], s[4:5], v94, s3, v[90:91]
	global_load_dwordx4 v[48:51], v[20:21], off
	global_load_dwordx4 v[52:55], v[20:21], off offset:32
	global_load_dwordx4 v[56:59], v[20:21], off offset:64
	global_load_dwordx4 v[60:63], v[20:21], off offset:96
	v_mad_u64_u32 v[22:23], s[4:5], v0, s85, v[84:85]
	ds_read_b128 v[0:3], v22
	ds_read_b128 v[16:19], v22 offset:32
	v_or_b32_e32 v20, s2, v86
	v_lshlrev_b32_e32 v21, 1, v20
	v_add_u32_e32 v26, v113, v21
	s_waitcnt vmcnt(3) lgkmcnt(1)
	v_mfma_f32_32x32x16_bf16 v[0:15], v[0:3], v[48:51], 0
	s_waitcnt vmcnt(2) lgkmcnt(0)
	v_mfma_f32_32x32x16_bf16 v[0:15], v[16:19], v[52:55], v[0:15]
	ds_read_b128 v[16:19], v22 offset:64
	ds_read_b128 v[22:25], v22 offset:96
	s_waitcnt vmcnt(1) lgkmcnt(1)
	v_mfma_f32_32x32x16_bf16 v[0:15], v[16:19], v[56:59], v[0:15]
	v_add_u32_e32 v16, 0xd800, v26
	ds_read2_b64 v[44:47], v16 offset1:2
	ds_read2_b64 v[36:39], v16 offset0:4 offset1:6
	v_add_u32_e32 v16, v114, v21
	v_add_u32_e32 v16, 0x6000, v16
	ds_read2_b64 v[40:43], v16 offset0:64 offset1:66
	ds_read2_b64 v[32:35], v16 offset0:68 offset1:70
	s_waitcnt vmcnt(0) lgkmcnt(4)
	v_mfma_f32_32x32x16_bf16 v[0:15], v[22:25], v[60:63], v[0:15]
	s_add_i32 s4, s2, s31
	s_cmpk_lt_u32 s4, 0x1000
	s_cselect_b64 s[4:5], -1, 0
	s_add_i32 s6, s28, s2
	s_cmpk_lt_u32 s6, 0x1000
	s_cselect_b64 s[6:7], -1, 0
	s_add_i32 s2, s72, s2
	s_cmpk_lt_u32 s2, 0x1000
	s_cselect_b64 s[12:13], -1, 0
	ds_read_b32 v17, v134
	ds_read_b32 v16, v134 offset:4
	ds_read_b32 v19, v134 offset:8
	ds_read_b32 v18, v134 offset:12
	ds_read_b32 v22, v134 offset:32
	ds_read_b32 v21, v134 offset:36
	ds_read_b32 v24, v134 offset:40
	ds_read_b32 v23, v134 offset:44
	ds_read_b32 v26, v134 offset:64
	ds_read_b32 v25, v134 offset:68
	ds_read_b32 v27, v134 offset:72
	ds_read_b32 v64, v134 offset:76
	ds_read_b32 v66, v134 offset:96
	ds_read_b32 v65, v134 offset:100
	ds_read_b32 v68, v134 offset:104
	ds_read_b32 v67, v134 offset:108
	s_waitcnt lgkmcnt(0)
; DI float other_half(float x, int h) { const u32x2 r = __builtin_amdgcn_permlane32_swap(__builtin_bit_cast(unsigned, x), __builtin_bit_cast(unsigned, x), false, false); return __builtin_bit_cast(float, h ? r.x : r.y); }
; DI int crow(int reg, int h) { return (reg & 3) + 8 * (reg >> 2) + 4 * h; }
; DI void phase_attn(const Frame& F, int j) {
;     ...
;                 for (int i = 0; i < 16; ++i) { const int kl = 32 * kt + crow(i, h); const int rel = kl - 128 - qrel; const int kp = q0 - 128 + kl;
;                     const bool ok = rel >= -128 && rel <= 128 && kp >= 0 && kp < SEQ;
;                     const int bi = rel < -128 ? 0 : (rel > 128 ? 256 : rel + 128);
;                     const float sc = ok ? x[i] * (0.125f * 1.44269504f) + bT[hh * 260 + bi] : -1e30f; x[i] = sc; mt = fmaxf(mt, sc); }
;                 }
;                 mt = fmaxf(mt, other_half(mt, h));
;                 if (__builtin_amdgcn_ballot_w64(mt > mrun + 8.f) != 0) {
;                     const float mnew = fmaxf(mrun, mt); const float alpha = __builtin_amdgcn_exp2f(mrun - mnew); lrun *= alpha; mrun = mnew;
; #pragma unroll
;                     for (int i = 0; i < 16; ++i) { O0[i] *= alpha; O1[i] *= alpha; } }
;                 float ps = 0.f;
; #pragma unroll
;                 for (int i = 0; i < 16; ++i) { const float p = __builtin_amdgcn_exp2f(x[i] - mrun); x[i] = p; ps += p; }
;                 lrun += ps;
; #pragma unroll
;                 for (int s = 0; s < 2; ++s) { const bf16x8 pf = pack_step(x, s);
;                     const bf16x8 v0 = __builtin_shufflevector(vf[s][0], vf[s][1], 0, 1, 2, 3, 4, 5, 6, 7), v1 = __builtin_shufflevector(vf[s][2], vf[s][3], 0, 1, 2, 3, 4, 5, 6, 7);
;                     O0 = __builtin_amdgcn_mfma_f32_32x32x16_bf16(v0, pf, O0, 0, 0, 0);
;                     O1 = __builtin_amdgcn_mfma_f32_32x32x16_bf16(v1, pf, O1, 0, 0, 0); }
	v_fmac_f32_e32 v17, 0x3e38aa3b, v0
	v_fmac_f32_e32 v16, 0x3e38aa3b, v1
	v_fmac_f32_e32 v19, 0x3e38aa3b, v2
	v_fmac_f32_e32 v18, 0x3e38aa3b, v3
	v_fmac_f32_e32 v22, 0x3e38aa3b, v4
	v_fmac_f32_e32 v21, 0x3e38aa3b, v5
	v_fmac_f32_e32 v24, 0x3e38aa3b, v6
	v_fmac_f32_e32 v23, 0x3e38aa3b, v7
	v_fmac_f32_e32 v26, 0x3e38aa3b, v8
	v_fmac_f32_e32 v25, 0x3e38aa3b, v9
	v_fmac_f32_e32 v27, 0x3e38aa3b, v10
	v_fmac_f32_e32 v64, 0x3e38aa3b, v11
	v_fmac_f32_e32 v66, 0x3e38aa3b, v12
	v_fmac_f32_e32 v65, 0x3e38aa3b, v13
	v_fmac_f32_e32 v68, 0x3e38aa3b, v14
	v_fmac_f32_e32 v67, 0x3e38aa3b, v15
	v_mov_b32_e32 v1, 0xf149f2ca
	s_and_b64 vcc, s[38:39], s[4:5]
	v_cndmask_b32_e32 v17, v1, v17, vcc
	s_and_b64 vcc, s[46:47], s[6:7]
	v_cndmask_b32_e32 v22, v1, v22, vcc
	s_and_b64 vcc, s[54:55], s[4:5]
	v_cndmask_b32_e32 v26, v1, v26, vcc
	s_and_b64 vcc, s[62:63], s[12:13]
	v_cndmask_b32_e32 v66, v1, v66, vcc
	v_add_u32_e32 v2, s90, v20
	v_add_u32_e32 v3, s91, v20
	v_add_u32_e32 v4, s10, v20
	v_cmp_gt_u32_e64 s[4:5], s11, v2
	v_cmp_gt_u32_e64 s[6:7], s11, v3
	v_cmp_gt_u32_e64 s[12:13], s11, v4
	s_and_b64 s[4:5], s[40:41], s[4:5]
	s_and_b64 s[6:7], s[42:43], s[6:7]
	s_and_b64 s[12:13], s[44:45], s[12:13]
	v_cndmask_b32_e64 v16, v1, v16, s[4:5]
	v_cndmask_b32_e64 v19, v1, v19, s[6:7]
	v_cndmask_b32_e64 v18, v1, v18, s[12:13]
	v_add_u32_e32 v2, s74, v20
	v_add_u32_e32 v3, s75, v20
	v_add_u32_e32 v4, s76, v20
	v_cmp_gt_u32_e64 s[4:5], s11, v2
	v_cmp_gt_u32_e64 s[6:7], s11, v3
	v_cmp_gt_u32_e64 s[12:13], s11, v4
	s_and_b64 s[4:5], s[48:49], s[4:5]
	s_and_b64 s[6:7], s[50:51], s[6:7]
	s_and_b64 s[12:13], s[52:53], s[12:13]
	v_cndmask_b32_e64 v21, v1, v21, s[4:5]
	v_cndmask_b32_e64 v24, v1, v24, s[6:7]
	v_cndmask_b32_e64 v23, v1, v23, s[12:13]
	v_add_u32_e32 v2, s77, v20
	v_add_u32_e32 v3, s80, v20
	v_add_u32_e32 v4, s81, v20
	v_cmp_gt_u32_e64 s[4:5], s11, v2
	v_cmp_gt_u32_e64 s[6:7], s11, v3
	v_cmp_gt_u32_e64 s[12:13], s11, v4
	s_and_b64 s[4:5], s[56:57], s[4:5]
	s_and_b64 s[6:7], s[58:59], s[6:7]
	s_and_b64 s[12:13], s[60:61], s[12:13]
	v_cndmask_b32_e64 v25, v1, v25, s[4:5]
	v_cndmask_b32_e64 v27, v1, v27, s[6:7]
	v_cndmask_b32_e64 v64, v1, v64, s[12:13]
	v_add_u32_e32 v2, s73, v20
	v_add_u32_e32 v3, s88, v20
	v_add_u32_e32 v4, s89, v20
	v_cmp_gt_u32_e64 s[4:5], s11, v2
	v_cmp_gt_u32_e64 s[6:7], s11, v3
	v_cmp_gt_u32_e64 s[12:13], s11, v4
	s_and_b64 s[4:5], s[64:65], s[4:5]
	s_and_b64 s[6:7], s[66:67], s[6:7]
	s_and_b64 s[12:13], s[68:69], s[12:13]
	v_cndmask_b32_e64 v65, v1, v65, s[4:5]
	v_cndmask_b32_e64 v68, v1, v68, s[6:7]
	v_cndmask_b32_e64 v67, v1, v67, s[12:13]
	v_max3_f32 v0, v17, s14, v16
	v_max3_f32 v0, v0, v19, v18
	v_max3_f32 v0, v0, v22, v21
	v_max3_f32 v0, v0, v24, v23
	v_max3_f32 v0, v0, v26, v25
	v_max3_f32 v0, v0, v27, v64
	v_max3_f32 v0, v0, v66, v65
	v_max3_f32 v0, v0, v68, v67
	v_mov_b32_e32 v1, v0
	v_mov_b32_e32 v2, v0
	s_nop 1
	v_permlane32_swap_b32_e32 v1, v2
	v_cndmask_b32_e64 v1, v1, v2, s[36:37]
	v_max_f32_e32 v1, v1, v1
	v_max_f32_e32 v0, v0, v1
	s_or_b32 s86, s82, 8
	v_cmp_gt_f32_e32 vcc, v0, v140
	v_max_f32_e32 v1, v139, v139
	s_cmp_eq_u64 vcc, 0
	v_max_f32_e32 v1, v1, v0
	s_cselect_b64 vcc, -1, 0
	v_cndmask_b32_e32 v143, v1, v139, vcc
	v_sub_f32_e32 v16, v16, v143
	v_exp_f32_e32 v75, v16
	v_sub_f32_e32 v16, v19, v143
	v_sub_f32_e32 v2, v139, v1
	v_exp_f32_e32 v76, v16
	v_sub_f32_e32 v16, v18, v143
	v_exp_f32_e32 v2, v2
	v_exp_f32_e32 v77, v16
	v_sub_f32_e32 v16, v22, v143
	v_exp_f32_e32 v78, v16
	v_sub_f32_e32 v16, v21, v143
	v_exp_f32_e32 v79, v16
	v_sub_f32_e32 v16, v24, v143
	v_exp_f32_e32 v96, v16
	v_sub_f32_e32 v16, v23, v143
	v_mul_f32_e32 v0, 0, v2
	v_exp_f32_e32 v97, v16
	v_sub_f32_e32 v16, v26, v143
	v_cndmask_b32_e64 v0, v0, 0, vcc
	v_exp_f32_e32 v98, v16
	v_sub_f32_e32 v16, v25, v143
	v_cndmask_b32_e64 v69, v2, 1.0, vcc
	v_mov_b32_e32 v1, v0
	v_mov_b32_e32 v2, v0
	v_mov_b32_e32 v3, v0
	v_mov_b32_e32 v4, v0
	v_mov_b32_e32 v5, v0
	v_mov_b32_e32 v6, v0
	v_mov_b32_e32 v7, v0
	v_mov_b32_e32 v8, v0
	v_mov_b32_e32 v9, v0
	v_mov_b32_e32 v10, v0
	v_mov_b32_e32 v11, v0
	v_mov_b32_e32 v12, v0
	v_mov_b32_e32 v13, v0
	v_mov_b32_e32 v14, v0
	v_mov_b32_e32 v15, v0
	v_sub_f32_e32 v17, v17, v143
	v_exp_f32_e32 v99, v16
	v_sub_f32_e32 v16, v27, v143
	v_exp_f32_e32 v74, v17
	v_exp_f32_e32 v100, v16
	s_nop 1
	v_cvt_pk_bf16_f32 v70, v74, v75
	v_cvt_pk_bf16_f32 v71, v76, v77
	v_cvt_pk_bf16_f32 v72, v78, v79
	v_cvt_pk_bf16_f32 v73, v96, v97
	s_nop 1
	s_add_i32 s70, s82, 1
	s_waitcnt lgkmcnt(3)
	v_mfma_f32_32x32x16_bf16 v[16:31], v[44:47], v[70:73], v[0:15]
	v_sub_f32_e32 v44, v64, v143
	v_sub_f32_e32 v45, v66, v143
	v_sub_f32_e32 v46, v65, v143
	v_sub_f32_e32 v47, v68, v143
	v_exp_f32_e32 v44, v44
	v_exp_f32_e32 v45, v45
	v_exp_f32_e32 v46, v46
	s_waitcnt lgkmcnt(1)
	v_mfma_f32_32x32x16_bf16 v[0:15], v[40:43], v[70:73], v[0:15]
	v_sub_f32_e32 v40, v67, v143
	v_exp_f32_e32 v47, v47
	v_exp_f32_e32 v64, v40
	s_nop 1
	v_cvt_pk_bf16_f32 v40, v98, v99
	v_cvt_pk_bf16_f32 v41, v100, v44
	v_cvt_pk_bf16_f32 v42, v45, v46
	v_cvt_pk_bf16_f32 v43, v47, v64
	s_nop 1
	v_ashrrev_i32_e32 v95, 31, v94
	s_mov_b32 s87, 0
	v_mov_b32_e32 v145, v141
	s_waitcnt lgkmcnt(0)
	v_mfma_f32_32x32x16_bf16 v[0:15], v[32:35], v[40:43], v[0:15]
	v_add_f32_e32 v32, 0, v74
	v_add_f32_e32 v32, v75, v32
	v_add_f32_e32 v32, v76, v32
	v_add_f32_e32 v32, v77, v32
	v_add_f32_e32 v32, v78, v32
	v_add_f32_e32 v32, v79, v32
	v_add_f32_e32 v32, v96, v32
	v_add_f32_e32 v32, v97, v32
	v_add_f32_e32 v32, v98, v32
	v_mfma_f32_32x32x16_bf16 v[16:31], v[36:39], v[40:43], v[16:31]
	v_add_f32_e32 v32, v99, v32
	v_add_f32_e32 v32, v100, v32
	v_add_f32_e32 v32, v44, v32
	v_add_f32_e32 v32, v45, v32
	v_add_f32_e32 v32, v46, v32
	v_add_f32_e32 v32, v47, v32
	v_add_f32_e32 v144, v64, v32
	v_fmac_f32_e32 v144, v112, v69
	v_mov_b32_e32 v146, v142
	v_mov_b32_e32 v147, v87
	s_mov_b32 s83, s70
	s_branch .LBB0_354
